# attention: exact early exit of the key-tile loop once the remaining-stick product C is exactly 0.0f for every row of the unit (per-wave flag via LDS at the per-tile barrier); later tiles contribute ex
# speedup vs baseline: 1.0312x; 1.0312x over previous
.LBB0_707:
	v_readfirstlane_b32 s58, v0
	s_nop 3
	s_lshr_b32 s58, s58, 6
	s_lshl_b32 s58, s58, 2
	s_add_i32 s58, s58, 0x11000
	s_ashr_i32 s26, s19, 4
	s_sub_i32 s6, 15, s26
	s_bfe_u32 s23, s19, 0x10003
	v_readfirstlane_b32 s21, v0
	s_lshl_b32 s27, s6, 8
	s_lshl_b32 s20, s6, 2
	s_lshl_b32 s6, s23, 12
	s_lshr_b32 s21, s21, 1
	s_add_i32 s6, s27, s6
	s_and_b32 s28, s21, 0x7fffffe0
	s_add_u32 s56, s28, s6
	s_addc_u32 s57, 0, 0
	v_mov_b32_e32 v5, s57
	v_or_b32_e32 v4, s56, v216
	v_readlane_b32 s24, v254, 54
	s_lshl_b32 s6, s19, 7
	v_lshlrev_b64 v[4:5], 11, v[4:5]
	v_readlane_b32 s25, v254, 55
	s_and_b32 s21, s6, 0x380
	s_lshl_b32 s6, s21, 1
	v_lshl_add_u64 v[4:5], s[24:25], 0, v[4:5]
	s_add_i32 s22, s20, 4
	s_lshl_b32 s23, s23, 23
	v_readlane_b32 s24, v255, 0
	s_add_u32 s24, s24, s23
	v_readlane_b32 s25, v255, 1
	s_addc_u32 s25, s25, 0
	s_add_u32 s24, s24, s6
	s_addc_u32 s25, s25, 0
	v_lshl_add_u64 v[186:187], s[24:25], 0, v[184:185]
	v_readlane_b32 s24, v254, 56
	v_readlane_b32 s25, v254, 57
	s_add_u32 s23, s24, s23
	s_addc_u32 s25, s25, 0
	s_add_u32 s24, s23, s6
	s_waitcnt vmcnt(11)
	v_lshl_add_u64 v[20:21], v[4:5], 0, s[6:7]
	s_addc_u32 s25, s25, 0
	s_or_b32 s6, s20, 3
	v_lshl_add_u64 v[188:189], s[24:25], 0, v[184:185]
	s_lshl_b64 s[24:25], s[6:7], 6
	v_mov_b32_e32 v5, s25
	v_or_b32_e32 v4, s24, v193
	v_mov_b32_e32 v7, s25
	v_or_b32_e32 v6, s24, v194
	v_lshlrev_b64 v[12:13], 11, v[4:5]
	v_lshlrev_b64 v[14:15], 11, v[6:7]
	v_lshl_add_u64 v[4:5], v[186:187], 0, v[12:13]
	v_lshl_add_u64 v[8:9], v[186:187], 0, v[14:15]
	v_lshl_add_u64 v[12:13], v[188:189], 0, v[12:13]
	v_lshl_add_u64 v[16:17], v[188:189], 0, v[14:15]
	global_load_dwordx4 v[4:7], v[4:5], off
	s_nop 0
	global_load_dwordx4 v[8:11], v[8:9], off
	s_nop 0
	global_load_dwordx4 v[12:15], v[12:13], off
	s_nop 0
	global_load_dwordx4 v[16:19], v[16:17], off
	s_or_b32 s6, s20, 2
	v_lshl_add_u64 v[20:21], v[20:21], 0, v[182:183]
	s_lshl_b64 s[24:25], s[6:7], 6
	s_or_b32 s6, s20, 1
	global_load_dwordx4 v[114:117], v[20:21], off
	global_load_dwordx4 v[118:121], v[20:21], off offset:32
	global_load_dwordx4 v[122:125], v[20:21], off offset:64
	global_load_dwordx4 v[126:129], v[20:21], off offset:96
	s_waitcnt lgkmcnt(0)
	global_load_dwordx4 v[130:133], v[20:21], off offset:128
	global_load_dwordx4 v[134:137], v[20:21], off offset:160
	global_load_dwordx4 v[138:141], v[20:21], off offset:192
	global_load_dwordx4 v[142:145], v[20:21], off offset:224
	v_mov_b32_e32 v21, s25
	v_or_b32_e32 v20, s24, v193
	s_waitcnt vmcnt(22)
	v_mov_b32_e32 v23, s25
	v_or_b32_e32 v22, s24, v194
	s_lshl_b64 s[24:25], s[6:7], 6
	v_lshlrev_b64 v[20:21], 11, v[20:21]
	v_mov_b32_e32 v25, s25
	v_or_b32_e32 v24, s24, v193
	s_waitcnt vmcnt(21)
	v_mov_b32_e32 v27, s25
	v_or_b32_e32 v26, s24, v194
	v_lshlrev_b64 v[22:23], 11, v[22:23]
	v_lshl_add_u64 v[28:29], v[186:187], 0, v[20:21]
	v_lshlrev_b64 v[24:25], 11, v[24:25]
	v_lshlrev_b64 v[26:27], 11, v[26:27]
	s_waitcnt vmcnt(20)
	v_lshl_add_u64 v[30:31], v[186:187], 0, v[22:23]
	v_lshl_add_u64 v[20:21], v[188:189], 0, v[20:21]
	v_lshl_add_u64 v[22:23], v[188:189], 0, v[22:23]
	v_lshl_add_u64 v[32:33], v[186:187], 0, v[24:25]
	s_waitcnt vmcnt(19)
	v_lshl_add_u64 v[34:35], v[186:187], 0, v[26:27]
	v_lshl_add_u64 v[24:25], v[188:189], 0, v[24:25]
	v_lshl_add_u64 v[26:27], v[188:189], 0, v[26:27]
	s_add_i32 s23, s28, s27
	s_lshl_b32 s6, s26, 8
	v_mov_b32_e32 v3, v2
	v_or_b32_e32 v234, s23, v216
	s_or_b32 s24, s23, 31
	s_sub_i32 s25, 0xf80, s6
	v_mov_b32_e32 v191, 1.0
	s_mov_b32 s6, s20
	s_mov_b32 s26, s7
	s_waitcnt vmcnt(11)
	ds_write_b128 v229, v[4:7]
	s_waitcnt vmcnt(10)
	ds_write_b128 v230, v[8:11]
	s_waitcnt vmcnt(9)
	ds_write_b128 v231, v[12:15] offset:32768
	s_waitcnt vmcnt(8)
	ds_write_b128 v232, v[16:19] offset:32768
	s_waitcnt lgkmcnt(0)
	s_barrier
	global_load_dwordx4 v[146:149], v[28:29], off
	global_load_dwordx4 v[150:153], v[30:31], off
	global_load_dwordx4 v[158:161], v[20:21], off
	global_load_dwordx4 v[166:169], v[22:23], off
	global_load_dwordx4 v[154:157], v[32:33], off
	global_load_dwordx4 v[162:165], v[34:35], off
	global_load_dwordx4 v[170:173], v[24:25], off
	global_load_dwordx4 v[174:177], v[26:27], off
	v_mov_b32_e32 v16, v2
	v_mov_b32_e32 v17, v2
	v_mov_b32_e32 v4, v2
	v_mov_b32_e32 v5, v2
	v_mov_b32_e32 v6, v2
	v_mov_b32_e32 v7, v2
	v_mov_b32_e32 v8, v2
	v_mov_b32_e32 v9, v2
	v_mov_b32_e32 v10, v2
	v_mov_b32_e32 v11, v2
	v_mov_b32_e32 v12, v2
	v_mov_b32_e32 v13, v2
	v_mov_b32_e32 v14, v2
	v_mov_b32_e32 v15, v2
	v_mov_b64_e32 v[32:33], v[16:17]
	v_mov_b64_e32 v[48:49], v[16:17]
	v_mov_b64_e32 v[64:65], v[16:17]
	v_mov_b64_e32 v[80:81], v[16:17]
	v_mov_b64_e32 v[30:31], v[14:15]
	v_mov_b64_e32 v[28:29], v[12:13]
	v_mov_b64_e32 v[26:27], v[10:11]
	v_mov_b64_e32 v[24:25], v[8:9]
	v_mov_b64_e32 v[22:23], v[6:7]
	v_mov_b64_e32 v[20:21], v[4:5]
	v_mov_b64_e32 v[18:19], v[2:3]
	v_mov_b64_e32 v[46:47], v[14:15]
	v_mov_b64_e32 v[44:45], v[12:13]
	v_mov_b64_e32 v[42:43], v[10:11]
	v_mov_b64_e32 v[40:41], v[8:9]
	v_mov_b64_e32 v[38:39], v[6:7]
	v_mov_b64_e32 v[36:37], v[4:5]
	v_mov_b64_e32 v[34:35], v[2:3]
	v_mov_b64_e32 v[62:63], v[14:15]
	v_mov_b64_e32 v[60:61], v[12:13]
	v_mov_b64_e32 v[58:59], v[10:11]
	v_mov_b64_e32 v[56:57], v[8:9]
	v_mov_b64_e32 v[54:55], v[6:7]
	v_mov_b64_e32 v[52:53], v[4:5]
	v_mov_b64_e32 v[50:51], v[2:3]
	v_mov_b64_e32 v[78:79], v[14:15]
	v_mov_b64_e32 v[76:77], v[12:13]
	v_mov_b64_e32 v[74:75], v[10:11]
	v_mov_b64_e32 v[72:73], v[8:9]
	v_mov_b64_e32 v[70:71], v[6:7]
	v_mov_b64_e32 v[68:69], v[4:5]
	v_mov_b64_e32 v[66:67], v[2:3]
	s_add_i32 s27, s25, 64
	s_cmp_ge_i32 s27, s24
	s_cbranch_scc1 .LBB0_712
	s_branch .LBB0_709

.Lsw0a_done:
	v_cmp_neq_f32_e32 vcc, 0, v191
	s_cmp_lg_u64 vcc, 0
	s_cselect_b32 s59, 1, 0
	v_mov_b32_e32 v4, s59
	v_mov_b32_e32 v5, s58
	ds_write_b32 v5, v4
	s_waitcnt lgkmcnt(0)
	s_barrier
	v_mov_b32_e32 v3, 0x11000
	ds_read_b128 v[4:7], v3
	ds_read_b128 v[8:11], v3 offset:16
	s_waitcnt lgkmcnt(0)
	v_or3_b32 v4, v4, v5, v6
	v_or3_b32 v4, v4, v7, v8
	v_or3_b32 v4, v4, v9, v10
	v_or_b32_e32 v4, v4, v11
	s_nop 1
	v_readfirstlane_b32 s59, v4
	s_nop 3
	s_cmp_eq_u32 s59, 0
	s_cbranch_scc1 .Late0_exit
	s_cmp_gt_u32 s26, s20
	s_cbranch_scc1 .LBB0_714
	s_lshl_b64 s[28:29], s[6:7], 6
	v_mov_b32_e32 v5, s29
	v_or_b32_e32 v4, s28, v193
	v_lshlrev_b64 v[4:5], 11, v[4:5]
	v_mov_b32_e32 v9, s29
	v_or_b32_e32 v8, s28, v194
	v_lshl_add_u64 v[6:7], v[186:187], 0, v[4:5]
	v_lshlrev_b64 v[8:9], 11, v[8:9]
	v_lshl_add_u64 v[4:5], v[188:189], 0, v[4:5]
	v_lshl_add_u64 v[10:11], v[186:187], 0, v[8:9]
	global_load_dwordx4 v[146:149], v[6:7], off
	global_load_dwordx4 v[150:153], v[10:11], off
	v_lshl_add_u64 v[6:7], v[188:189], 0, v[8:9]
	global_load_dwordx4 v[158:161], v[4:5], off
	global_load_dwordx4 v[166:169], v[6:7], off

.LBB0_720:
	v_cmp_neq_f32_e32 vcc, 0, v191
	s_cmp_lg_u64 vcc, 0
	s_cselect_b32 s59, 1, 0
	v_mov_b32_e32 v4, s59
	v_mov_b32_e32 v5, s58
	ds_write_b32 v5, v4 offset:32
	s_waitcnt lgkmcnt(0)
	s_barrier
	v_mov_b32_e32 v3, 0x11020
	ds_read_b128 v[4:7], v3
	ds_read_b128 v[8:11], v3 offset:16
	s_waitcnt lgkmcnt(0)
	v_or3_b32 v4, v4, v5, v6
	v_or3_b32 v4, v4, v7, v8
	v_or3_b32 v4, v4, v9, v10
	v_or_b32_e32 v4, v4, v11
	s_nop 1
	v_readfirstlane_b32 s59, v4
	s_nop 3
	s_cmp_eq_u32 s59, 0
	s_cbranch_scc1 .Late0_exit
	s_cmp_ge_u32 s26, s20
	s_cbranch_scc1 .LBB0_722
	s_add_i32 s30, s6, -1
	s_ashr_i32 s31, s30, 31
	s_lshl_b64 s[30:31], s[30:31], 6
	v_mov_b32_e32 v5, s31
	v_or_b32_e32 v4, s30, v193
	v_lshlrev_b64 v[4:5], 11, v[4:5]
	v_mov_b32_e32 v9, s31
	v_or_b32_e32 v8, s30, v194
	v_lshl_add_u64 v[6:7], v[186:187], 0, v[4:5]
	v_lshlrev_b64 v[8:9], 11, v[8:9]
	v_lshl_add_u64 v[4:5], v[188:189], 0, v[4:5]
	v_lshl_add_u64 v[10:11], v[186:187], 0, v[8:9]
	global_load_dwordx4 v[154:157], v[6:7], off
	global_load_dwordx4 v[162:165], v[10:11], off
	v_lshl_add_u64 v[6:7], v[188:189], 0, v[8:9]
	global_load_dwordx4 v[170:173], v[4:5], off
	global_load_dwordx4 v[174:177], v[6:7], off

.Late0_exit:
	s_waitcnt vmcnt(0)
	s_lshl_b64 s[22:23], s[56:57], 11
	s_add_u32 s6, s92, s22
	s_addc_u32 s22, s93, s23
	s_lshl_b32 s20, s21, 1
	s_add_u32 s20, s6, s20
	s_addc_u32 s21, s22, 0
	v_lshlrev_b32_e32 v4, 1, v216
	v_mov_b32_e32 v5, v2
	v_lshl_add_u64 v[4:5], s[20:21], 0, v[4:5]
	v_lshl_add_u64 v[4:5], v[4:5], 0, v[180:181]
	v_cvt_pk_bf16_f32 v3, v66, s0
	global_store_short v[4:5], v3, off
	v_cvt_pk_bf16_f32 v3, v50, s0
	global_store_short v[4:5], v3, off offset:64
	v_cvt_pk_bf16_f32 v3, v34, s0
	global_store_short v[4:5], v3, off offset:128
	v_cvt_pk_bf16_f32 v3, v18, s0
	global_store_short v[4:5], v3, off offset:192
	v_cvt_pk_bf16_f32 v3, v67, s0
	global_store_short v[4:5], v3, off offset:2048
	v_cvt_pk_bf16_f32 v3, v51, s0
	global_store_short v[4:5], v3, off offset:2112
	v_cvt_pk_bf16_f32 v3, v35, s0
	global_store_short v[4:5], v3, off offset:2176
	v_cvt_pk_bf16_f32 v3, v19, s0
	v_add_co_u32_e32 v6, vcc, s12, v4
	global_store_short v[4:5], v3, off offset:2240
	v_cvt_pk_bf16_f32 v3, v68, s0
	v_addc_co_u32_e32 v7, vcc, 0, v5, vcc
	global_store_short v[6:7], v3, off
	v_cvt_pk_bf16_f32 v3, v52, s0
	global_store_short v[6:7], v3, off offset:64
	v_cvt_pk_bf16_f32 v3, v36, s0
	global_store_short v[6:7], v3, off offset:128
	v_cvt_pk_bf16_f32 v3, v20, s0
	global_store_short v[6:7], v3, off offset:192
	v_cvt_pk_bf16_f32 v3, v69, s0
	global_store_short v[6:7], v3, off offset:2048
	v_cvt_pk_bf16_f32 v3, v53, s0
	global_store_short v[6:7], v3, off offset:2112
	v_cvt_pk_bf16_f32 v3, v37, s0
	global_store_short v[6:7], v3, off offset:2176
	v_cvt_pk_bf16_f32 v3, v21, s0
	global_store_short v[6:7], v3, off offset:2240
	v_add_co_u32_e32 v6, vcc, s13, v4
	v_cvt_pk_bf16_f32 v3, v70, s0
	s_nop 0
	v_addc_co_u32_e32 v7, vcc, 0, v5, vcc
	v_add_co_u32_e32 v8, vcc, s16, v4
	s_add_i32 s19, s19, s9
	s_nop 0
	v_addc_co_u32_e32 v9, vcc, 0, v5, vcc
	global_store_short v[8:9], v3, off offset:-4096
	v_cvt_pk_bf16_f32 v3, v54, s0
	global_store_short v[6:7], v3, off offset:64
	v_cvt_pk_bf16_f32 v3, v38, s0
	global_store_short v[6:7], v3, off offset:128
	v_cvt_pk_bf16_f32 v3, v22, s0
	global_store_short v[6:7], v3, off offset:192
	v_cvt_pk_bf16_f32 v3, v71, s0
	global_store_short v[6:7], v3, off offset:2048
	v_cvt_pk_bf16_f32 v3, v55, s0
	global_store_short v[6:7], v3, off offset:2112
	v_cvt_pk_bf16_f32 v3, v39, s0
	global_store_short v[6:7], v3, off offset:2176
	v_cvt_pk_bf16_f32 v3, v23, s0
	global_store_short v[6:7], v3, off offset:2240
	v_cvt_pk_bf16_f32 v3, v72, s0
	global_store_short v[8:9], v3, off
	v_cvt_pk_bf16_f32 v3, v56, s0
	global_store_short v[8:9], v3, off offset:64
	v_cvt_pk_bf16_f32 v3, v40, s0
	global_store_short v[8:9], v3, off offset:128
	v_cvt_pk_bf16_f32 v3, v24, s0
	global_store_short v[8:9], v3, off offset:192
	v_cvt_pk_bf16_f32 v3, v73, s0
	global_store_short v[8:9], v3, off offset:2048
	v_cvt_pk_bf16_f32 v3, v57, s0
	global_store_short v[8:9], v3, off offset:2112
	v_cvt_pk_bf16_f32 v3, v41, s0
	v_add_co_u32_e32 v6, vcc, s10, v4
	global_store_short v[8:9], v3, off offset:2176
	v_cvt_pk_bf16_f32 v3, v25, s0
	v_addc_co_u32_e32 v7, vcc, 0, v5, vcc
	global_store_short v[8:9], v3, off offset:2240
	v_add_co_u32_e32 v8, vcc, s17, v4
	v_cvt_pk_bf16_f32 v3, v74, s0
	s_nop 0
	v_addc_co_u32_e32 v9, vcc, 0, v5, vcc
	global_store_short v[8:9], v3, off offset:-4096
	v_cvt_pk_bf16_f32 v3, v58, s0
	global_store_short v[6:7], v3, off offset:64
	v_cvt_pk_bf16_f32 v3, v42, s0
	global_store_short v[6:7], v3, off offset:128
	v_cvt_pk_bf16_f32 v3, v26, s0
	global_store_short v[6:7], v3, off offset:192
	v_cvt_pk_bf16_f32 v3, v75, s0
	global_store_short v[6:7], v3, off offset:2048
	v_cvt_pk_bf16_f32 v3, v59, s0
	global_store_short v[6:7], v3, off offset:2112
	v_cvt_pk_bf16_f32 v3, v43, s0
	global_store_short v[6:7], v3, off offset:2176
	v_cvt_pk_bf16_f32 v3, v27, s0
	global_store_short v[6:7], v3, off offset:2240
	v_cvt_pk_bf16_f32 v3, v76, s0
	global_store_short v[8:9], v3, off
	v_cvt_pk_bf16_f32 v3, v60, s0
	global_store_short v[8:9], v3, off offset:64
	v_cvt_pk_bf16_f32 v3, v44, s0
	global_store_short v[8:9], v3, off offset:128
	v_cvt_pk_bf16_f32 v3, v28, s0
	global_store_short v[8:9], v3, off offset:192
	v_cvt_pk_bf16_f32 v3, v77, s0
	global_store_short v[8:9], v3, off offset:2048
	v_cvt_pk_bf16_f32 v3, v61, s0
	v_add_co_u32_e32 v6, vcc, s11, v4
	global_store_short v[8:9], v3, off offset:2112
	v_cvt_pk_bf16_f32 v3, v45, s0
	v_addc_co_u32_e32 v7, vcc, 0, v5, vcc
	global_store_short v[8:9], v3, off offset:2176
	v_cvt_pk_bf16_f32 v3, v29, s0
	v_add_co_u32_e32 v4, vcc, s18, v4
	global_store_short v[8:9], v3, off offset:2240
	v_cvt_pk_bf16_f32 v3, v78, s0
	v_addc_co_u32_e32 v5, vcc, 0, v5, vcc
	global_store_short v[4:5], v3, off offset:-4096
	v_cvt_pk_bf16_f32 v3, v62, s0
	global_store_short v[6:7], v3, off offset:64
	v_cvt_pk_bf16_f32 v3, v46, s0
	global_store_short v[6:7], v3, off offset:128
	v_cvt_pk_bf16_f32 v3, v30, s0
	global_store_short v[6:7], v3, off offset:192
	v_cvt_pk_bf16_f32 v3, v79, s0
	global_store_short v[6:7], v3, off offset:2048
	v_cvt_pk_bf16_f32 v3, v63, s0
	global_store_short v[6:7], v3, off offset:2112
	v_cvt_pk_bf16_f32 v3, v47, s0
	global_store_short v[6:7], v3, off offset:2176
	v_cvt_pk_bf16_f32 v3, v31, s0
	global_store_short v[6:7], v3, off offset:2240
	v_cvt_pk_bf16_f32 v3, v80, s0
	global_store_short v[4:5], v3, off
	v_cvt_pk_bf16_f32 v3, v64, s0
	global_store_short v[4:5], v3, off offset:64
	v_cvt_pk_bf16_f32 v3, v48, s0
	global_store_short v[4:5], v3, off offset:128
	v_cvt_pk_bf16_f32 v3, v32, s0
	global_store_short v[4:5], v3, off offset:192
	v_cvt_pk_bf16_f32 v3, v81, s0
	global_store_short v[4:5], v3, off offset:2048
	v_cvt_pk_bf16_f32 v3, v65, s0
	global_store_short v[4:5], v3, off offset:2112
	v_cvt_pk_bf16_f32 v3, v49, s0
	global_store_short v[4:5], v3, off offset:2176
	v_cvt_pk_bf16_f32 v3, v33, s0
	s_cmpk_gt_i32 s19, 0xff
	global_store_short v[4:5], v3, off offset:2240
	s_cbranch_scc0 .LBB0_707

.LBB0_2275:
	v_readfirstlane_b32 s58, v0
	s_nop 3
	s_lshr_b32 s58, s58, 6
	s_lshl_b32 s58, s58, 2
	s_add_i32 s58, s58, 0x11000
	s_ashr_i32 s31, s23, 4
	s_sub_i32 s6, 15, s31
	s_bfe_u32 s26, s23, 0x10003
	v_readfirstlane_b32 s20, v0
	s_lshl_b32 s29, s6, 8
	s_lshl_b32 s24, s6, 2
	s_lshl_b32 s6, s26, 12
	s_lshr_b32 s20, s20, 1
	s_add_i32 s6, s29, s6
	s_and_b32 s30, s20, 0x7fffffe0
	s_add_u32 s20, s30, s6
	s_addc_u32 s21, 0, 0
	s_lshl_b32 s6, s23, 7
	s_and_b32 s25, s6, 0x380
	s_lshl_b32 s6, s25, 1
	s_add_i32 s28, s24, 4
	s_lshl_b32 s33, s26, 23
	v_readlane_b32 s26, v255, 0
	s_add_u32 s26, s26, s33
	v_readlane_b32 s27, v255, 1
	s_addc_u32 s27, s27, 0
	s_add_u32 s26, s26, s6
	s_addc_u32 s27, s27, 0
	v_lshl_add_u64 v[186:187], s[26:27], 0, v[184:185]
	v_readlane_b32 s26, v254, 56
	v_mov_b32_e32 v5, s21
	v_or_b32_e32 v4, s20, v216
	v_readlane_b32 s34, v254, 54
	v_readlane_b32 s27, v254, 57
	s_add_u32 s26, s26, s33
	v_lshlrev_b64 v[4:5], 11, v[4:5]
	v_readlane_b32 s35, v254, 55
	s_addc_u32 s27, s27, 0
	s_add_u32 s26, s26, s6
	v_lshl_add_u64 v[4:5], s[34:35], 0, v[4:5]
	s_waitcnt vmcnt(11)
	v_lshl_add_u64 v[20:21], v[4:5], 0, s[6:7]
	s_addc_u32 s27, s27, 0
	s_or_b32 s6, s24, 3
	v_lshl_add_u64 v[188:189], s[26:27], 0, v[184:185]
	s_lshl_b64 s[26:27], s[6:7], 6
	v_mov_b32_e32 v5, s27
	v_or_b32_e32 v4, s26, v193
	v_mov_b32_e32 v7, s27
	v_or_b32_e32 v6, s26, v194
	v_lshlrev_b64 v[12:13], 11, v[4:5]
	v_lshlrev_b64 v[14:15], 11, v[6:7]
	v_lshl_add_u64 v[4:5], v[186:187], 0, v[12:13]
	v_lshl_add_u64 v[8:9], v[186:187], 0, v[14:15]
	v_lshl_add_u64 v[12:13], v[188:189], 0, v[12:13]
	v_lshl_add_u64 v[16:17], v[188:189], 0, v[14:15]
	global_load_dwordx4 v[4:7], v[4:5], off
	s_nop 0
	global_load_dwordx4 v[8:11], v[8:9], off
	s_nop 0
	global_load_dwordx4 v[12:15], v[12:13], off
	s_nop 0
	global_load_dwordx4 v[16:19], v[16:17], off
	s_or_b32 s6, s24, 2
	v_lshl_add_u64 v[20:21], v[20:21], 0, v[182:183]
	s_lshl_b64 s[26:27], s[6:7], 6
	s_or_b32 s6, s24, 1
	global_load_dwordx4 v[114:117], v[20:21], off
	global_load_dwordx4 v[118:121], v[20:21], off offset:32
	global_load_dwordx4 v[122:125], v[20:21], off offset:64
	global_load_dwordx4 v[126:129], v[20:21], off offset:96
	s_waitcnt lgkmcnt(0)
	global_load_dwordx4 v[130:133], v[20:21], off offset:128
	global_load_dwordx4 v[134:137], v[20:21], off offset:160
	global_load_dwordx4 v[138:141], v[20:21], off offset:192
	global_load_dwordx4 v[142:145], v[20:21], off offset:224
	v_mov_b32_e32 v21, s27
	v_or_b32_e32 v20, s26, v193
	s_waitcnt vmcnt(22)
	v_mov_b32_e32 v23, s27
	v_or_b32_e32 v22, s26, v194
	s_lshl_b64 s[26:27], s[6:7], 6
	v_lshlrev_b64 v[20:21], 11, v[20:21]
	v_mov_b32_e32 v25, s27
	v_or_b32_e32 v24, s26, v193
	s_waitcnt vmcnt(21)
	v_mov_b32_e32 v27, s27
	v_or_b32_e32 v26, s26, v194
	v_lshlrev_b64 v[22:23], 11, v[22:23]
	v_lshl_add_u64 v[28:29], v[186:187], 0, v[20:21]
	v_lshlrev_b64 v[24:25], 11, v[24:25]
	v_lshlrev_b64 v[26:27], 11, v[26:27]
	s_waitcnt vmcnt(20)
	v_lshl_add_u64 v[30:31], v[186:187], 0, v[22:23]
	v_lshl_add_u64 v[20:21], v[188:189], 0, v[20:21]
	v_lshl_add_u64 v[22:23], v[188:189], 0, v[22:23]
	v_lshl_add_u64 v[32:33], v[186:187], 0, v[24:25]
	s_waitcnt vmcnt(19)
	v_lshl_add_u64 v[34:35], v[186:187], 0, v[26:27]
	v_lshl_add_u64 v[24:25], v[188:189], 0, v[24:25]
	v_lshl_add_u64 v[26:27], v[188:189], 0, v[26:27]
	s_add_i32 s29, s30, s29
	s_lshl_b32 s6, s31, 8
	v_mov_b32_e32 v3, v2
	v_or_b32_e32 v234, s29, v216
	s_or_b32 s30, s29, 31
	s_sub_i32 s31, 0xf80, s6
	v_mov_b32_e32 v191, 1.0
	s_mov_b32 s6, s24
	s_mov_b32 s33, s7
	s_waitcnt vmcnt(11)
	ds_write_b128 v229, v[4:7]
	s_waitcnt vmcnt(10)
	ds_write_b128 v230, v[8:11]
	s_waitcnt vmcnt(9)
	ds_write_b128 v231, v[12:15] offset:32768
	s_waitcnt vmcnt(8)
	ds_write_b128 v232, v[16:19] offset:32768
	s_waitcnt lgkmcnt(0)
	s_barrier
	global_load_dwordx4 v[146:149], v[28:29], off
	global_load_dwordx4 v[150:153], v[30:31], off
	global_load_dwordx4 v[158:161], v[20:21], off
	global_load_dwordx4 v[166:169], v[22:23], off
	global_load_dwordx4 v[154:157], v[32:33], off
	global_load_dwordx4 v[162:165], v[34:35], off
	global_load_dwordx4 v[170:173], v[24:25], off
	global_load_dwordx4 v[174:177], v[26:27], off
	v_mov_b32_e32 v16, v2
	v_mov_b32_e32 v17, v2
	v_mov_b32_e32 v4, v2
	v_mov_b32_e32 v5, v2
	v_mov_b32_e32 v6, v2
	v_mov_b32_e32 v7, v2
	v_mov_b32_e32 v8, v2
	v_mov_b32_e32 v9, v2
	v_mov_b32_e32 v10, v2
	v_mov_b32_e32 v11, v2
	v_mov_b32_e32 v12, v2
	v_mov_b32_e32 v13, v2
	v_mov_b32_e32 v14, v2
	v_mov_b32_e32 v15, v2
	v_mov_b64_e32 v[32:33], v[16:17]
	v_mov_b64_e32 v[48:49], v[16:17]
	v_mov_b64_e32 v[64:65], v[16:17]
	v_mov_b64_e32 v[80:81], v[16:17]
	v_mov_b64_e32 v[30:31], v[14:15]
	v_mov_b64_e32 v[28:29], v[12:13]
	v_mov_b64_e32 v[26:27], v[10:11]
	v_mov_b64_e32 v[24:25], v[8:9]
	v_mov_b64_e32 v[22:23], v[6:7]
	v_mov_b64_e32 v[20:21], v[4:5]
	v_mov_b64_e32 v[18:19], v[2:3]
	v_mov_b64_e32 v[46:47], v[14:15]
	v_mov_b64_e32 v[44:45], v[12:13]
	v_mov_b64_e32 v[42:43], v[10:11]
	v_mov_b64_e32 v[40:41], v[8:9]
	v_mov_b64_e32 v[38:39], v[6:7]
	v_mov_b64_e32 v[36:37], v[4:5]
	v_mov_b64_e32 v[34:35], v[2:3]
	v_mov_b64_e32 v[62:63], v[14:15]
	v_mov_b64_e32 v[60:61], v[12:13]
	v_mov_b64_e32 v[58:59], v[10:11]
	v_mov_b64_e32 v[56:57], v[8:9]
	v_mov_b64_e32 v[54:55], v[6:7]
	v_mov_b64_e32 v[52:53], v[4:5]
	v_mov_b64_e32 v[50:51], v[2:3]
	v_mov_b64_e32 v[78:79], v[14:15]
	v_mov_b64_e32 v[76:77], v[12:13]
	v_mov_b64_e32 v[74:75], v[10:11]
	v_mov_b64_e32 v[72:73], v[8:9]
	v_mov_b64_e32 v[70:71], v[6:7]
	v_mov_b64_e32 v[68:69], v[4:5]
	v_mov_b64_e32 v[66:67], v[2:3]
	s_add_i32 s26, s31, 64
	s_cmp_ge_i32 s26, s30
	s_cbranch_scc1 .LBB0_2280
	s_branch .LBB0_2277

.Lsw1a_done:
	v_cmp_neq_f32_e32 vcc, 0, v191
	s_cmp_lg_u64 vcc, 0
	s_cselect_b32 s59, 1, 0
	v_mov_b32_e32 v4, s59
	v_mov_b32_e32 v5, s58
	ds_write_b32 v5, v4
	s_waitcnt lgkmcnt(0)
	s_barrier
	v_mov_b32_e32 v3, 0x11000
	ds_read_b128 v[4:7], v3
	ds_read_b128 v[8:11], v3 offset:16
	s_waitcnt lgkmcnt(0)
	v_or3_b32 v4, v4, v5, v6
	v_or3_b32 v4, v4, v7, v8
	v_or3_b32 v4, v4, v9, v10
	v_or_b32_e32 v4, v4, v11
	s_nop 1
	v_readfirstlane_b32 s59, v4
	s_nop 3
	s_cmp_eq_u32 s59, 0
	s_cbranch_scc1 .Late1_exit
	s_cmp_gt_u32 s33, s24
	s_cbranch_scc1 .LBB0_2282
	s_lshl_b64 s[26:27], s[6:7], 6
	v_mov_b32_e32 v5, s27
	v_or_b32_e32 v4, s26, v193
	v_lshlrev_b64 v[4:5], 11, v[4:5]
	v_mov_b32_e32 v9, s27
	v_or_b32_e32 v8, s26, v194
	v_lshl_add_u64 v[6:7], v[186:187], 0, v[4:5]
	v_lshlrev_b64 v[8:9], 11, v[8:9]
	v_lshl_add_u64 v[4:5], v[188:189], 0, v[4:5]
	v_lshl_add_u64 v[10:11], v[186:187], 0, v[8:9]
	global_load_dwordx4 v[146:149], v[6:7], off
	global_load_dwordx4 v[150:153], v[10:11], off
	v_lshl_add_u64 v[6:7], v[188:189], 0, v[8:9]
	global_load_dwordx4 v[158:161], v[4:5], off
	global_load_dwordx4 v[166:169], v[6:7], off

.LBB0_2288:
	v_cmp_neq_f32_e32 vcc, 0, v191
	s_cmp_lg_u64 vcc, 0
	s_cselect_b32 s59, 1, 0
	v_mov_b32_e32 v4, s59
	v_mov_b32_e32 v5, s58
	ds_write_b32 v5, v4 offset:32
	s_waitcnt lgkmcnt(0)
	s_barrier
	v_mov_b32_e32 v3, 0x11020
	ds_read_b128 v[4:7], v3
	ds_read_b128 v[8:11], v3 offset:16
	s_waitcnt lgkmcnt(0)
	v_or3_b32 v4, v4, v5, v6
	v_or3_b32 v4, v4, v7, v8
	v_or3_b32 v4, v4, v9, v10
	v_or_b32_e32 v4, v4, v11
	s_nop 1
	v_readfirstlane_b32 s59, v4
	s_nop 3
	s_cmp_eq_u32 s59, 0
	s_cbranch_scc1 .Late1_exit
	s_cmp_ge_u32 s33, s24
	s_cbranch_scc1 .LBB0_2290
	s_add_i32 s52, s6, -1
	s_ashr_i32 s53, s52, 31
	s_lshl_b64 s[52:53], s[52:53], 6
	v_mov_b32_e32 v5, s53
	v_or_b32_e32 v4, s52, v193
	v_lshlrev_b64 v[4:5], 11, v[4:5]
	v_mov_b32_e32 v9, s53
	v_or_b32_e32 v8, s52, v194
	v_lshl_add_u64 v[6:7], v[186:187], 0, v[4:5]
	v_lshlrev_b64 v[8:9], 11, v[8:9]
	v_lshl_add_u64 v[4:5], v[188:189], 0, v[4:5]
	v_lshl_add_u64 v[10:11], v[186:187], 0, v[8:9]
	global_load_dwordx4 v[154:157], v[6:7], off
	global_load_dwordx4 v[162:165], v[10:11], off
	v_lshl_add_u64 v[6:7], v[188:189], 0, v[8:9]
	global_load_dwordx4 v[170:173], v[4:5], off
	global_load_dwordx4 v[174:177], v[6:7], off

.Late1_exit:
	s_waitcnt vmcnt(0)
	s_lshl_b64 s[20:21], s[20:21], 11
	v_readlane_b32 s6, v255, 4
	s_add_u32 s6, s6, s20
	v_readlane_b32 s20, v255, 2
	s_addc_u32 s21, s20, s21
	s_lshl_b32 s20, s25, 1
	s_add_u32 s20, s6, s20
	s_addc_u32 s21, s21, 0
	v_lshlrev_b32_e32 v4, 1, v216
	v_mov_b32_e32 v5, v2
	v_lshl_add_u64 v[4:5], s[20:21], 0, v[4:5]
	v_lshl_add_u64 v[4:5], v[4:5], 0, v[180:181]
	v_cvt_pk_bf16_f32 v3, v66, s0
	global_store_short v[4:5], v3, off
	v_cvt_pk_bf16_f32 v3, v50, s0
	global_store_short v[4:5], v3, off offset:64
	v_cvt_pk_bf16_f32 v3, v34, s0
	global_store_short v[4:5], v3, off offset:128
	v_cvt_pk_bf16_f32 v3, v18, s0
	global_store_short v[4:5], v3, off offset:192
	v_cvt_pk_bf16_f32 v3, v67, s0
	global_store_short v[4:5], v3, off offset:2048
	v_cvt_pk_bf16_f32 v3, v51, s0
	global_store_short v[4:5], v3, off offset:2112
	v_cvt_pk_bf16_f32 v3, v35, s0
	global_store_short v[4:5], v3, off offset:2176
	v_cvt_pk_bf16_f32 v3, v19, s0
	v_add_co_u32_e32 v6, vcc, s16, v4
	global_store_short v[4:5], v3, off offset:2240
	v_cvt_pk_bf16_f32 v3, v68, s0
	v_addc_co_u32_e32 v7, vcc, 0, v5, vcc
	global_store_short v[6:7], v3, off
	v_cvt_pk_bf16_f32 v3, v52, s0
	global_store_short v[6:7], v3, off offset:64
	v_cvt_pk_bf16_f32 v3, v36, s0
	global_store_short v[6:7], v3, off offset:128
	v_cvt_pk_bf16_f32 v3, v20, s0
	global_store_short v[6:7], v3, off offset:192
	v_cvt_pk_bf16_f32 v3, v69, s0
	global_store_short v[6:7], v3, off offset:2048
	v_cvt_pk_bf16_f32 v3, v53, s0
	global_store_short v[6:7], v3, off offset:2112
	v_cvt_pk_bf16_f32 v3, v37, s0
	global_store_short v[6:7], v3, off offset:2176
	v_cvt_pk_bf16_f32 v3, v21, s0
	global_store_short v[6:7], v3, off offset:2240
	v_add_co_u32_e32 v6, vcc, s17, v4
	v_cvt_pk_bf16_f32 v3, v70, s0
	s_nop 0
	v_addc_co_u32_e32 v7, vcc, 0, v5, vcc
	v_add_co_u32_e32 v8, vcc, s18, v4
	s_add_i32 s23, s23, s9
	s_nop 0
	v_addc_co_u32_e32 v9, vcc, 0, v5, vcc
	global_store_short v[8:9], v3, off offset:-4096
	v_cvt_pk_bf16_f32 v3, v54, s0
	global_store_short v[6:7], v3, off offset:64
	v_cvt_pk_bf16_f32 v3, v38, s0
	global_store_short v[6:7], v3, off offset:128
	v_cvt_pk_bf16_f32 v3, v22, s0
	global_store_short v[6:7], v3, off offset:192
	v_cvt_pk_bf16_f32 v3, v71, s0
	global_store_short v[6:7], v3, off offset:2048
	v_cvt_pk_bf16_f32 v3, v55, s0
	global_store_short v[6:7], v3, off offset:2112
	v_cvt_pk_bf16_f32 v3, v39, s0
	global_store_short v[6:7], v3, off offset:2176
	v_cvt_pk_bf16_f32 v3, v23, s0
	global_store_short v[6:7], v3, off offset:2240
	v_cvt_pk_bf16_f32 v3, v72, s0
	global_store_short v[8:9], v3, off
	v_cvt_pk_bf16_f32 v3, v56, s0
	global_store_short v[8:9], v3, off offset:64
	v_cvt_pk_bf16_f32 v3, v40, s0
	global_store_short v[8:9], v3, off offset:128
	v_cvt_pk_bf16_f32 v3, v24, s0
	global_store_short v[8:9], v3, off offset:192
	v_cvt_pk_bf16_f32 v3, v73, s0
	global_store_short v[8:9], v3, off offset:2048
	v_cvt_pk_bf16_f32 v3, v57, s0
	global_store_short v[8:9], v3, off offset:2112
	v_cvt_pk_bf16_f32 v3, v41, s0
	v_add_co_u32_e32 v6, vcc, s10, v4
	global_store_short v[8:9], v3, off offset:2176
	v_cvt_pk_bf16_f32 v3, v25, s0
	v_addc_co_u32_e32 v7, vcc, 0, v5, vcc
	global_store_short v[8:9], v3, off offset:2240
	v_add_co_u32_e32 v8, vcc, s19, v4
	v_cvt_pk_bf16_f32 v3, v74, s0
	s_nop 0
	v_addc_co_u32_e32 v9, vcc, 0, v5, vcc
	global_store_short v[8:9], v3, off offset:-4096
	v_cvt_pk_bf16_f32 v3, v58, s0
	global_store_short v[6:7], v3, off offset:64
	v_cvt_pk_bf16_f32 v3, v42, s0
	global_store_short v[6:7], v3, off offset:128
	v_cvt_pk_bf16_f32 v3, v26, s0
	global_store_short v[6:7], v3, off offset:192
	v_cvt_pk_bf16_f32 v3, v75, s0
	global_store_short v[6:7], v3, off offset:2048
	v_cvt_pk_bf16_f32 v3, v59, s0
	global_store_short v[6:7], v3, off offset:2112
	v_cvt_pk_bf16_f32 v3, v43, s0
	global_store_short v[6:7], v3, off offset:2176
	v_cvt_pk_bf16_f32 v3, v27, s0
	global_store_short v[6:7], v3, off offset:2240
	v_cvt_pk_bf16_f32 v3, v76, s0
	global_store_short v[8:9], v3, off
	v_cvt_pk_bf16_f32 v3, v60, s0
	global_store_short v[8:9], v3, off offset:64
	v_cvt_pk_bf16_f32 v3, v44, s0
	global_store_short v[8:9], v3, off offset:128
	v_cvt_pk_bf16_f32 v3, v28, s0
	global_store_short v[8:9], v3, off offset:192
	v_cvt_pk_bf16_f32 v3, v77, s0
	global_store_short v[8:9], v3, off offset:2048
	v_cvt_pk_bf16_f32 v3, v61, s0
	v_add_co_u32_e32 v6, vcc, s11, v4
	global_store_short v[8:9], v3, off offset:2112
	v_cvt_pk_bf16_f32 v3, v45, s0
	v_addc_co_u32_e32 v7, vcc, 0, v5, vcc
	global_store_short v[8:9], v3, off offset:2176
	v_cvt_pk_bf16_f32 v3, v29, s0
	v_add_co_u32_e32 v4, vcc, s22, v4
	global_store_short v[8:9], v3, off offset:2240
	v_cvt_pk_bf16_f32 v3, v78, s0
	v_addc_co_u32_e32 v5, vcc, 0, v5, vcc
	global_store_short v[4:5], v3, off offset:-4096
	v_cvt_pk_bf16_f32 v3, v62, s0
	global_store_short v[6:7], v3, off offset:64
	v_cvt_pk_bf16_f32 v3, v46, s0
	global_store_short v[6:7], v3, off offset:128
	v_cvt_pk_bf16_f32 v3, v30, s0
	global_store_short v[6:7], v3, off offset:192
	v_cvt_pk_bf16_f32 v3, v79, s0
	global_store_short v[6:7], v3, off offset:2048
	v_cvt_pk_bf16_f32 v3, v63, s0
	global_store_short v[6:7], v3, off offset:2112
	v_cvt_pk_bf16_f32 v3, v47, s0
	global_store_short v[6:7], v3, off offset:2176
	v_cvt_pk_bf16_f32 v3, v31, s0
	global_store_short v[6:7], v3, off offset:2240
	v_cvt_pk_bf16_f32 v3, v80, s0
	global_store_short v[4:5], v3, off
	v_cvt_pk_bf16_f32 v3, v64, s0
	global_store_short v[4:5], v3, off offset:64
	v_cvt_pk_bf16_f32 v3, v48, s0
	global_store_short v[4:5], v3, off offset:128
	v_cvt_pk_bf16_f32 v3, v32, s0
	global_store_short v[4:5], v3, off offset:192
	v_cvt_pk_bf16_f32 v3, v81, s0
	global_store_short v[4:5], v3, off offset:2048
	v_cvt_pk_bf16_f32 v3, v65, s0
	global_store_short v[4:5], v3, off offset:2112
	v_cvt_pk_bf16_f32 v3, v49, s0
	global_store_short v[4:5], v3, off offset:2176
	v_cvt_pk_bf16_f32 v3, v33, s0
	s_cmpk_gt_i32 s23, 0xff
	global_store_short v[4:5], v3, off offset:2240
	s_cbranch_scc0 .LBB0_2275
